# NSA block ranking: broadcasts issued back to back, rank counted by 64-bit key compares; NSA ticket requested one unit ahead; barrier leader releases its XCD before its own invalidate
# baseline (speedup 1.0000x reference)
.LBB0_372:
	s_or_b64 exec, exec, s[4:5]
	s_mov_b64 s[4:5], exec
	v_mbcnt_lo_u32_b32 v2, s4, 0
	v_mbcnt_hi_u32_b32 v2, s5, v2
	v_cmp_eq_u32_e32 vcc, 0, v2
	s_waitcnt vmcnt(0)
	s_and_saveexec_b64 s[8:9], vcc
	s_cbranch_execz .LBB0_374
	s_bcnt1_i32_b64 s4, s[4:5]
	v_mov_b32_e32 v2, s4
	v_readlane_b32 s4, v253, 55
	v_readlane_b32 s5, v253, 56
	s_nop 4
	global_atomic_add v3, v2, s[4:5]
.LBB0_374:
	s_or_b64 exec, exec, s[8:9]
	buffer_inv sc1
	s_waitcnt vmcnt(0)
	s_mov_b64 s[4:5], exec

.LBB0_603:
	s_or_b64 exec, exec, s[2:3]
	s_mov_b64 s[2:3], exec
	v_mbcnt_lo_u32_b32 v2, s2, 0
	v_mbcnt_hi_u32_b32 v2, s3, v2
	v_cmp_eq_u32_e32 vcc, 0, v2
	s_waitcnt vmcnt(0)
	s_and_saveexec_b64 s[8:9], vcc
	s_cbranch_execz .LBB0_605
	s_bcnt1_i32_b64 s2, s[2:3]
	v_mov_b32_e32 v2, s2
	v_readlane_b32 s2, v253, 55
	v_readlane_b32 s3, v253, 56
	s_nop 4
	global_atomic_add v3, v2, s[2:3]
.LBB0_605:
	s_or_b64 exec, exec, s[8:9]
	buffer_inv sc1
	s_waitcnt vmcnt(0)
	s_mov_b64 s[2:3], exec

.LBB0_633:
	v_readlane_b32 s48, v253, 1
	v_readlane_b32 s49, v253, 2
	s_load_dword s0, s[48:49], 0xd8
	v_readlane_b32 s2, v254, 5
	v_readlane_b32 s3, v254, 6
	s_xor_b64 s[2:3], s[2:3], -1
	v_writelane_b32 v254, s2, 13
	s_add_i32 s1, s66, 2
	s_waitcnt lgkmcnt(0)
	s_cmp_lt_i32 s1, s0
	v_writelane_b32 v254, s3, 14
	v_writelane_b32 v254, s66, 15
	s_cbranch_scc1 .LBB0_894
	s_load_dword s0, s[48:49], 0xdc
	s_waitcnt lgkmcnt(0)
	v_writelane_b32 v254, s0, 16
	s_cmp_gt_i32 s1, s0
	s_cbranch_scc1 .LBB0_894
	s_load_dwordx2 s[2:3], s[48:49], 0xd0
	v_writelane_b32 v254, s1, 17
	s_nop 0
	v_readlane_b32 s0, v254, 7
	v_readlane_b32 s1, v254, 8
	s_lshl_b32 s82, s0, 9
	s_lshl_b64 s[0:1], s[82:83], 2
	s_waitcnt lgkmcnt(0)
	s_add_u32 s0, s2, s0
	s_addc_u32 s1, s3, s1
	v_writelane_b32 v254, s0, 18
	s_add_u32 s0, s0, 0x4400
	v_writelane_b32 v254, s1, 19
	s_addc_u32 s1, s1, 0
	s_add_u32 s50, s2, 0x26ac2000
	v_writelane_b32 v254, s0, 20
	s_addc_u32 s51, s3, 0
	s_nop 0
	v_writelane_b32 v254, s1, 21
	s_add_u32 s0, s2, 0x49ac2000
	v_writelane_b32 v254, s0, 22
	s_addc_u32 s0, s3, 0
	v_writelane_b32 v254, s0, 23
	s_add_u32 s0, s2, 0x47ac2000
	s_addc_u32 s1, s3, 0
	v_writelane_b32 v254, s0, 24
	s_nop 1
	v_writelane_b32 v254, s1, 25
	s_add_u32 s0, s2, 0x43ac2000
	s_addc_u32 s1, s3, 0
	v_writelane_b32 v254, s0, 26
	s_nop 1
	v_writelane_b32 v254, s1, 27
	s_add_u32 s0, s2, 0x1aaa2000
	v_writelane_b32 v254, s0, 28
	s_addc_u32 s0, s3, 0
	v_writelane_b32 v254, s0, 29
	s_add_u32 s0, s2, 0x1a6a2000
	v_writelane_b32 v254, s0, 30
	s_addc_u32 s0, s3, 0
	v_writelane_b32 v254, s0, 31
	s_add_u32 s0, s2, 0x22a2000
	v_writelane_b32 v254, s0, 32
	s_addc_u32 s0, s3, 0
	v_writelane_b32 v254, s0, 33
	s_add_u32 s0, s2, 0x1ca2000
	v_writelane_b32 v254, s0, 34
	s_addc_u32 s0, s3, 0
	v_writelane_b32 v254, s0, 35
	s_add_u32 s0, s2, 0x862000
	v_writelane_b32 v254, s0, 36
	v_writelane_b32 v254, s2, 37
	s_addc_u32 s0, s3, 0
	s_nop 0
	v_writelane_b32 v254, s3, 38
	v_writelane_b32 v254, s0, 39
	v_writelane_b32 v254, s48, 40
	s_nop 1
	v_writelane_b32 v254, s49, 41
	v_writelane_b32 v254, s50, 42
	s_nop 1
	v_writelane_b32 v254, s51, 43
	v_cmp_eq_u32_e32 vcc, 0, v0
	s_and_saveexec_b64 s[84:85], vcc
	s_cbranch_execz .Lnsa_tk_skip
	v_readlane_b32 s86, v254, 20
	v_readlane_b32 s87, v254, 21
	v_mov_b32_e32 v251, 1
	s_nop 3
	global_atomic_add v251, v3, v251, s[86:87] sc0
.Lnsa_tk_skip:
	s_or_b64 exec, exec, s[84:85]
	s_branch .LBB0_638

.LBB0_638:
	s_setprio 0
	v_mov_b32_e32 v2, v0
	s_waitcnt vmcnt(0)
	s_barrier
	s_nop 0
	v_cmp_eq_u32_e32 vcc, 0, v2
	s_and_saveexec_b64 s[0:1], vcc
	s_cbranch_execz .LBB0_642
	v_mov_b32_e32 v4, s73
	ds_write_b32 v4, v251
	v_readlane_b32 s4, v254, 20
	v_readlane_b32 s5, v254, 21
	v_mov_b32_e32 v251, 1
	s_nop 3
	global_atomic_add v251, v3, v251, s[4:5] sc0

.LBB0_652:
	v_writelane_b32 v255, s19, 26
	v_writelane_b32 v255, s16, 27
	s_nop 1
	v_writelane_b32 v255, s17, 28
	v_writelane_b32 v255, s15, 29
	v_writelane_b32 v255, s11, 30
	v_writelane_b32 v255, s9, 31
	v_writelane_b32 v255, s8, 32
	v_writelane_b32 v255, s14, 33
	v_writelane_b32 v255, s12, 34
	s_or_b64 exec, exec, s[0:1]
	s_sub_i32 s0, 30, s18
	v_cmp_eq_u32_e64 s[2:3], 0, v129
	v_cmp_eq_u32_e32 vcc, s6, v129
	v_writelane_b32 v254, s0, 46
	v_cmp_eq_u32_e64 s[4:5], s0, v129
	s_or_b64 s[0:1], vcc, s[4:5]
	v_writelane_b32 v254, s2, 47
	s_nor_b64 s[0:1], s[2:3], s[0:1]
	s_lshl_b32 s82, s13, 6
	v_writelane_b32 v254, s3, 48
	v_writelane_b32 v254, s0, 49
	s_cmp_lg_u32 s18, 31
	v_cmp_ne_u32_e32 vcc, 1, v129
	v_writelane_b32 v254, s1, 50
	v_cmp_ge_u32_e64 s[0:1], s6, v129
	v_writelane_b32 v255, s13, 35
	v_writelane_b32 v255, s82, 36
	v_writelane_b32 v254, s0, 51
	v_lshlrev_b32_e32 v11, 2, v65
	v_writelane_b32 v255, s83, 37
	v_writelane_b32 v254, s1, 52
	v_cmp_eq_u32_e64 s[0:1], 0, v69
	v_and_b32_e32 v11, 0x80, v11
	v_lshlrev_b32_e32 v130, 3, v68
	v_writelane_b32 v254, s0, 53
	v_or_b32_e32 v10, 2, v67
	v_or_b32_e32 v9, 4, v67
	v_writelane_b32 v254, s1, 54
	v_cmp_ne_u32_e64 s[0:1], 0, v129
	v_or_b32_e32 v8, 6, v67
	v_mov_b32_e32 v131, v3
	v_writelane_b32 v254, s0, 55
	s_mov_b32 s33, 0
	v_or_b32_e32 v12, 4, v11
	v_writelane_b32 v254, s1, 56
	v_cmp_lt_u32_e64 s[0:1], 1, v129
	v_or_b32_e32 v13, 8, v11
	v_or_b32_e32 v14, 12, v11
	v_writelane_b32 v254, s0, 57
	v_or_b32_e32 v15, 16, v11
	v_or_b32_e32 v16, 20, v11
	v_writelane_b32 v254, s1, 58
	s_cselect_b64 s[0:1], -1, 0
	v_writelane_b32 v254, s18, 59
	s_and_b64 s[0:1], s[0:1], vcc
	v_writelane_b32 v254, s0, 60
	s_cmp_gt_u32 s6, 1
	v_cmp_ne_u32_e32 vcc, 2, v129
	v_writelane_b32 v254, s1, 61
	v_cmp_lt_u32_e64 s[0:1], 2, v129
	v_or_b32_e32 v17, 24, v11
	v_or_b32_e32 v50, 28, v11
	v_writelane_b32 v254, s0, 62
	v_or_b32_e32 v51, 32, v11
	v_or_b32_e32 v52, 36, v11
	v_writelane_b32 v254, s1, 63
	s_cselect_b64 s[0:1], -1, 0
	s_and_b64 s[0:1], s[0:1], vcc
	v_writelane_b32 v255, s0, 0
	s_cmp_gt_u32 s6, 2
	v_cmp_ne_u32_e32 vcc, 3, v129
	v_writelane_b32 v255, s1, 1
	v_cmp_lt_u32_e64 s[0:1], 3, v129
	v_or_b32_e32 v53, 40, v11
	v_or_b32_e32 v54, 44, v11
	v_writelane_b32 v255, s0, 2
	v_or_b32_e32 v55, 48, v11
	v_or_b32_e32 v56, 52, v11
	v_writelane_b32 v255, s1, 3
	s_cselect_b64 s[0:1], -1, 0
	s_and_b64 s[0:1], s[0:1], vcc
	v_writelane_b32 v255, s0, 4
	s_cmp_gt_u32 s6, 3
	v_cmp_ne_u32_e32 vcc, 4, v129
	v_writelane_b32 v255, s1, 5
	v_cmp_lt_u32_e64 s[0:1], 4, v129
	v_or_b32_e32 v57, 56, v11
	v_or_b32_e32 v58, 60, v11
	v_writelane_b32 v255, s0, 6
	v_or_b32_e32 v59, 64, v11
	v_or_b32_e32 v60, 0x44, v11
	v_writelane_b32 v255, s1, 7
	s_cselect_b64 s[0:1], -1, 0
	s_and_b64 s[0:1], s[0:1], vcc
	v_writelane_b32 v255, s0, 8
	s_cmp_gt_u32 s6, 4
	v_cmp_ne_u32_e32 vcc, 5, v129
	v_writelane_b32 v255, s1, 9
	v_cmp_lt_u32_e64 s[0:1], 5, v129
	v_or_b32_e32 v61, 0x48, v11
	v_or_b32_e32 v62, 0x4c, v11
	v_writelane_b32 v255, s0, 10
	v_or_b32_e32 v63, 0x50, v11
	v_or_b32_e32 v68, 0x54, v11
	v_writelane_b32 v255, s1, 11
	s_cselect_b64 s[0:1], -1, 0
	s_and_b64 s[0:1], s[0:1], vcc
	v_writelane_b32 v255, s0, 12
	s_cmp_gt_u32 s6, 5
	v_cmp_ne_u32_e32 vcc, 6, v129
	v_writelane_b32 v255, s1, 13
	v_cmp_lt_u32_e64 s[0:1], 6, v129
	v_or_b32_e32 v69, 0x58, v11
	v_or_b32_e32 v70, 0x5c, v11
	v_writelane_b32 v255, s0, 14
	v_or_b32_e32 v71, 0x60, v11
	v_or_b32_e32 v72, 0x64, v11
	v_writelane_b32 v255, s1, 15
	s_cselect_b64 s[0:1], -1, 0
	s_and_b64 s[0:1], s[0:1], vcc
	v_writelane_b32 v255, s0, 16
	s_cmp_gt_u32 s6, 6
	v_cmp_ne_u32_e32 vcc, 7, v129
	v_writelane_b32 v255, s1, 17
	v_cmp_lt_u32_e64 s[0:1], 7, v129
	v_or_b32_e32 v73, 0x68, v11
	v_or_b32_e32 v74, 0x6c, v11
	v_writelane_b32 v255, s0, 18
	v_or_b32_e32 v75, 0x70, v11
	v_or_b32_e32 v76, 0x74, v11
	v_writelane_b32 v255, s1, 19
	s_cselect_b64 s[0:1], -1, 0
	s_and_b64 s[0:1], s[0:1], vcc
	v_writelane_b32 v255, s0, 20
	s_cmp_gt_u32 s6, 7
	v_cmp_ne_u32_e32 vcc, 8, v129
	v_writelane_b32 v255, s1, 21
	v_cmp_lt_u32_e64 s[0:1], 8, v129
	v_or_b32_e32 v77, 0x78, v11
	v_or_b32_e32 v78, 0x7c, v11
	v_writelane_b32 v255, s0, 22
	v_cmp_lt_u32_e64 s[60:61], 9, v129
	v_cmp_lt_u32_e64 s[62:63], 10, v129
	v_writelane_b32 v255, s1, 23
	s_cselect_b64 s[0:1], -1, 0
	s_and_b64 s[0:1], s[0:1], vcc
	v_writelane_b32 v255, s0, 24
	s_cmp_gt_u32 s6, 8
	v_cmp_ne_u32_e32 vcc, 9, v129
	v_writelane_b32 v255, s1, 25
	s_cselect_b64 s[0:1], -1, 0
	s_and_b64 s[18:19], s[0:1], vcc
	s_cmp_gt_u32 s6, 9
	v_cmp_ne_u32_e32 vcc, 10, v129
	s_cselect_b64 s[0:1], -1, 0
	s_and_b64 s[24:25], s[0:1], vcc
	s_cmp_gt_u32 s6, 10
	v_cmp_ne_u32_e32 vcc, 11, v129
	s_cselect_b64 s[0:1], -1, 0
	s_and_b64 s[14:15], s[0:1], vcc
	s_cmp_gt_u32 s6, 11
	v_cmp_ne_u32_e32 vcc, 12, v129
	s_cselect_b64 s[0:1], -1, 0
	s_and_b64 s[36:37], s[0:1], vcc
	s_cmp_gt_u32 s6, 12
	v_cmp_ne_u32_e32 vcc, 13, v129
	s_cselect_b64 s[0:1], -1, 0
	s_and_b64 s[26:27], s[0:1], vcc
	s_cmp_gt_u32 s6, 13
	v_cmp_ne_u32_e32 vcc, 14, v129
	s_cselect_b64 s[0:1], -1, 0
	s_and_b64 s[40:41], s[0:1], vcc
	s_cmp_gt_u32 s6, 14
	v_cmp_ne_u32_e32 vcc, 15, v129
	s_cselect_b64 s[0:1], -1, 0
	s_and_b64 s[20:21], s[0:1], vcc
	s_cmp_gt_u32 s6, 15
	v_cmp_ne_u32_e32 vcc, 16, v129
	s_cselect_b64 s[0:1], -1, 0
	s_and_b64 s[38:39], s[0:1], vcc
	s_cmp_gt_u32 s6, 16
	v_cmp_ne_u32_e32 vcc, 17, v129
	s_cselect_b64 s[0:1], -1, 0
	s_and_b64 s[10:11], s[0:1], vcc
	s_cmp_gt_u32 s6, 17
	v_cmp_ne_u32_e32 vcc, 18, v129
	s_cselect_b64 s[0:1], -1, 0
	s_and_b64 s[42:43], s[0:1], vcc
	s_cmp_gt_u32 s6, 18
	v_cmp_ne_u32_e32 vcc, 19, v129
	s_cselect_b64 s[0:1], -1, 0
	s_and_b64 s[44:45], s[0:1], vcc
	s_cmp_gt_u32 s6, 19
	v_cmp_ne_u32_e32 vcc, 20, v129
	s_cselect_b64 s[0:1], -1, 0
	s_and_b64 s[12:13], s[0:1], vcc
	s_cmp_gt_u32 s6, 20
	v_cmp_ne_u32_e32 vcc, 21, v129
	s_cselect_b64 s[0:1], -1, 0
	s_and_b64 s[46:47], s[0:1], vcc
	s_cmp_gt_u32 s6, 21
	v_cmp_ne_u32_e32 vcc, 22, v129
	s_cselect_b64 s[0:1], -1, 0
	s_and_b64 s[2:3], s[0:1], vcc
	s_cmp_gt_u32 s6, 22
	v_cmp_ne_u32_e32 vcc, 23, v129
	s_cselect_b64 s[0:1], -1, 0
	s_and_b64 s[48:49], s[0:1], vcc
	s_cmp_gt_u32 s6, 23
	v_cmp_ne_u32_e32 vcc, 24, v129
	s_cselect_b64 s[0:1], -1, 0
	s_and_b64 s[0:1], s[0:1], vcc
	s_cmp_gt_u32 s6, 24
	v_cmp_ne_u32_e32 vcc, 25, v129
	s_cselect_b64 s[4:5], -1, 0
	s_and_b64 s[50:51], s[4:5], vcc
	s_cmp_gt_u32 s6, 25
	v_cmp_ne_u32_e32 vcc, 26, v129
	s_cselect_b64 s[4:5], -1, 0
	s_and_b64 s[28:29], s[4:5], vcc
	s_cmp_gt_u32 s6, 26
	v_cmp_ne_u32_e32 vcc, 27, v129
	s_cselect_b64 s[4:5], -1, 0
	s_and_b64 s[52:53], s[4:5], vcc
	s_cmp_gt_u32 s6, 27
	v_cmp_ne_u32_e32 vcc, 28, v129
	s_cselect_b64 s[4:5], -1, 0
	s_and_b64 s[16:17], s[4:5], vcc
	s_cmp_gt_u32 s6, 28
	v_cmp_ne_u32_e32 vcc, 29, v129
	s_cselect_b64 s[4:5], -1, 0
	s_and_b64 s[54:55], s[4:5], vcc
	s_cmp_gt_u32 s6, 29
	v_cmp_ne_u32_e32 vcc, 30, v129
	s_cselect_b64 s[4:5], -1, 0
	s_and_b64 s[22:23], s[4:5], vcc
	s_cmp_gt_u32 s6, 30
	v_cmp_ne_u32_e32 vcc, 31, v129
	s_cselect_b64 s[4:5], -1, 0
	s_and_b64 s[56:57], s[4:5], vcc
	v_cmp_lt_u32_e64 s[64:65], 11, v129
	v_cmp_lt_u32_e64 s[66:67], 12, v129
	v_cmp_lt_u32_e64 s[68:69], 13, v129
	v_cmp_lt_u32_e64 s[70:71], 14, v129
	v_cmp_lt_u32_e64 s[72:73], 15, v129
	v_cmp_lt_u32_e64 s[74:75], 16, v129
	v_cmp_lt_u32_e64 s[76:77], 17, v129
	v_cmp_lt_u32_e64 s[78:79], 18, v129
	v_cmp_lt_u32_e64 s[80:81], 19, v129
	v_cmp_lt_u32_e64 s[82:83], 20, v129
	v_cmp_lt_u32_e64 s[84:85], 21, v129
	v_cmp_lt_u32_e64 s[86:87], 22, v129
	v_cmp_lt_u32_e64 s[88:89], 23, v129
	v_cmp_lt_u32_e64 s[90:91], 24, v129
	v_cmp_lt_u32_e64 s[92:93], 25, v129
	v_cmp_lt_u32_e64 s[94:95], 26, v129
	v_cmp_lt_u32_e64 s[96:97], 27, v129
	v_cmp_lt_u32_e64 s[4:5], 28, v129
	v_cmp_lt_u32_e64 s[6:7], 29, v129
	v_cmp_eq_u32_e64 s[8:9], 31, v129
	s_waitcnt lgkmcnt(0)
	s_barrier
	v_mov_b32_e32 v82, 31
	v_mov_b32_e32 v84, 30
	v_mov_b32_e32 v86, 29
	v_mov_b32_e32 v88, 28
	v_mov_b32_e32 v90, 27
	v_mov_b32_e32 v92, 26
	v_mov_b32_e32 v94, 25
	v_mov_b32_e32 v96, 24
	v_mov_b32_e32 v114, 23
	v_mov_b32_e32 v116, 22
	v_mov_b32_e32 v118, 21
	v_mov_b32_e32 v120, 20
	v_mov_b32_e32 v136, 19
	v_mov_b32_e32 v138, 18
	v_mov_b32_e32 v140, 17
	v_mov_b32_e32 v168, 16
	v_mov_b32_e32 v170, 15
	v_mov_b32_e32 v172, 14
	v_mov_b32_e32 v174, 13
	v_mov_b32_e32 v176, 12
	v_mov_b32_e32 v178, 11
	v_mov_b32_e32 v206, 10
	v_mov_b32_e32 v208, 9
	v_mov_b32_e32 v210, 8
	v_mov_b32_e32 v212, 7
	v_mov_b32_e32 v214, 6
	v_mov_b32_e32 v216, 5
	v_mov_b32_e32 v218, 4
	v_mov_b32_e32 v222, 3
	v_mov_b32_e32 v224, 2
	v_mov_b32_e32 v226, 1
	v_mov_b32_e32 v228, 0
	v_sub_u32_e32 v230, 31, v129
	s_branch .LBB0_654

.LBB0_654:
	v_lshl_add_u32 v79, s33, 9, v65
	v_readlane_b32 s30, v254, 49
	v_ashrrev_i32_e32 v79, 5, v79
	v_mov_b32_e32 v80, 0x7f800000
	v_readlane_b32 s31, v254, 50
	s_and_saveexec_b64 s[34:35], s[30:31]
	s_movk_i32 s30, 0x84
	v_mad_u64_u32 v[80:81], s[58:59], v79, s30, v[2:3]
	ds_read_b32 v80, v80
	s_or_b64 exec, exec, s[34:35]
	s_waitcnt lgkmcnt(0)
	v_readlane_b32 s30, v254, 51
	v_readlane_b32 s31, v254, 52
	v_mov_b32_e32 v231, v80
	v_mov_b32_e32 v233, 0
	v_cndmask_b32_e64 v232, 0, v80, s[30:31]
	ds_bpermute_b32 v83, v11, v232
	ds_bpermute_b32 v85, v12, v232
	ds_bpermute_b32 v87, v13, v232
	ds_bpermute_b32 v89, v14, v232
	ds_bpermute_b32 v91, v15, v232
	ds_bpermute_b32 v93, v16, v232
	ds_bpermute_b32 v95, v17, v232
	ds_bpermute_b32 v97, v50, v232
	ds_bpermute_b32 v115, v51, v232
	ds_bpermute_b32 v117, v52, v232
	ds_bpermute_b32 v119, v53, v232
	ds_bpermute_b32 v121, v54, v232
	ds_bpermute_b32 v137, v55, v232
	ds_bpermute_b32 v139, v56, v232
	ds_bpermute_b32 v141, v57, v232
	s_waitcnt lgkmcnt(14)
	v_cmp_gt_u64_e64 s[84:85], v[82:83], v[230:231]
	ds_bpermute_b32 v169, v58, v232
	s_waitcnt lgkmcnt(14)
	v_cmp_gt_u64_e64 s[86:87], v[84:85], v[230:231]
	ds_bpermute_b32 v171, v59, v232
	s_waitcnt lgkmcnt(14)
	v_cmp_gt_u64_e64 s[88:89], v[86:87], v[230:231]
	ds_bpermute_b32 v173, v60, v232
	v_addc_co_u32_e64 v233, s[34:35], 0, v233, s[84:85]
	s_waitcnt lgkmcnt(14)
	v_cmp_gt_u64_e64 s[90:91], v[88:89], v[230:231]
	ds_bpermute_b32 v175, v61, v232
	v_addc_co_u32_e64 v233, s[34:35], 0, v233, s[86:87]
	s_waitcnt lgkmcnt(14)
	v_cmp_gt_u64_e64 s[92:93], v[90:91], v[230:231]
	ds_bpermute_b32 v177, v62, v232
	v_addc_co_u32_e64 v233, s[34:35], 0, v233, s[88:89]
	s_waitcnt lgkmcnt(14)
	v_cmp_gt_u64_e64 s[94:95], v[92:93], v[230:231]
	ds_bpermute_b32 v179, v63, v232
	v_addc_co_u32_e64 v233, s[34:35], 0, v233, s[90:91]
	s_waitcnt lgkmcnt(14)
	v_cmp_gt_u64_e64 s[96:97], v[94:95], v[230:231]
	ds_bpermute_b32 v207, v68, v232
	v_addc_co_u32_e64 v233, s[34:35], 0, v233, s[92:93]
	s_waitcnt lgkmcnt(14)
	v_cmp_gt_u64_e64 s[84:85], v[96:97], v[230:231]
	ds_bpermute_b32 v209, v69, v232
	v_addc_co_u32_e64 v233, s[34:35], 0, v233, s[94:95]
	s_waitcnt lgkmcnt(14)
	v_cmp_gt_u64_e64 s[86:87], v[114:115], v[230:231]
	ds_bpermute_b32 v211, v70, v232
	v_addc_co_u32_e64 v233, s[34:35], 0, v233, s[96:97]
	s_waitcnt lgkmcnt(14)
	v_cmp_gt_u64_e64 s[88:89], v[116:117], v[230:231]
	ds_bpermute_b32 v213, v71, v232
	v_addc_co_u32_e64 v233, s[34:35], 0, v233, s[84:85]
	s_waitcnt lgkmcnt(14)
	v_cmp_gt_u64_e64 s[90:91], v[118:119], v[230:231]
	ds_bpermute_b32 v215, v72, v232
	v_addc_co_u32_e64 v233, s[34:35], 0, v233, s[86:87]
	s_waitcnt lgkmcnt(14)
	v_cmp_gt_u64_e64 s[92:93], v[120:121], v[230:231]
	ds_bpermute_b32 v217, v73, v232
	v_addc_co_u32_e64 v233, s[34:35], 0, v233, s[88:89]
	s_waitcnt lgkmcnt(14)
	v_cmp_gt_u64_e64 s[94:95], v[136:137], v[230:231]
	ds_bpermute_b32 v219, v74, v232
	v_addc_co_u32_e64 v233, s[34:35], 0, v233, s[90:91]
	s_waitcnt lgkmcnt(14)
	v_cmp_gt_u64_e64 s[96:97], v[138:139], v[230:231]
	ds_bpermute_b32 v223, v75, v232
	v_addc_co_u32_e64 v233, s[34:35], 0, v233, s[92:93]
	s_waitcnt lgkmcnt(14)
	v_cmp_gt_u64_e64 s[84:85], v[140:141], v[230:231]
	ds_bpermute_b32 v225, v76, v232
	v_addc_co_u32_e64 v233, s[34:35], 0, v233, s[94:95]
	s_waitcnt lgkmcnt(14)
	v_cmp_gt_u64_e64 s[86:87], v[168:169], v[230:231]
	ds_bpermute_b32 v227, v77, v232
	v_addc_co_u32_e64 v233, s[34:35], 0, v233, s[96:97]
	s_waitcnt lgkmcnt(14)
	v_cmp_gt_u64_e64 s[88:89], v[170:171], v[230:231]
	ds_bpermute_b32 v229, v78, v232
	v_addc_co_u32_e64 v233, s[34:35], 0, v233, s[84:85]
	s_waitcnt lgkmcnt(14)
	v_cmp_gt_u64_e64 s[90:91], v[172:173], v[230:231]
	v_addc_co_u32_e64 v233, s[34:35], 0, v233, s[86:87]
	s_waitcnt lgkmcnt(13)
	v_cmp_gt_u64_e64 s[92:93], v[174:175], v[230:231]
	v_addc_co_u32_e64 v233, s[34:35], 0, v233, s[88:89]
	s_waitcnt lgkmcnt(12)
	v_cmp_gt_u64_e64 s[94:95], v[176:177], v[230:231]
	v_addc_co_u32_e64 v233, s[34:35], 0, v233, s[90:91]
	s_waitcnt lgkmcnt(11)
	v_cmp_gt_u64_e64 s[96:97], v[178:179], v[230:231]
	v_addc_co_u32_e64 v233, s[34:35], 0, v233, s[92:93]
	s_waitcnt lgkmcnt(10)
	v_cmp_gt_u64_e64 s[84:85], v[206:207], v[230:231]
	v_addc_co_u32_e64 v233, s[34:35], 0, v233, s[94:95]
	s_waitcnt lgkmcnt(9)
	v_cmp_gt_u64_e64 s[86:87], v[208:209], v[230:231]
	v_addc_co_u32_e64 v233, s[34:35], 0, v233, s[96:97]
	s_waitcnt lgkmcnt(8)
	v_cmp_gt_u64_e64 s[88:89], v[210:211], v[230:231]
	v_addc_co_u32_e64 v233, s[34:35], 0, v233, s[84:85]
	s_waitcnt lgkmcnt(7)
	v_cmp_gt_u64_e64 s[90:91], v[212:213], v[230:231]
	v_addc_co_u32_e64 v233, s[34:35], 0, v233, s[86:87]
	s_waitcnt lgkmcnt(6)
	v_cmp_gt_u64_e64 s[92:93], v[214:215], v[230:231]
	v_addc_co_u32_e64 v233, s[34:35], 0, v233, s[88:89]
	s_waitcnt lgkmcnt(5)
	v_cmp_gt_u64_e64 s[94:95], v[216:217], v[230:231]
	v_addc_co_u32_e64 v233, s[34:35], 0, v233, s[90:91]
	s_waitcnt lgkmcnt(4)
	v_cmp_gt_u64_e64 s[96:97], v[218:219], v[230:231]
	v_addc_co_u32_e64 v233, s[34:35], 0, v233, s[92:93]
	s_waitcnt lgkmcnt(3)
	v_cmp_gt_u64_e64 s[84:85], v[222:223], v[230:231]
	v_addc_co_u32_e64 v233, s[34:35], 0, v233, s[94:95]
	s_waitcnt lgkmcnt(2)
	v_cmp_gt_u64_e64 s[86:87], v[224:225], v[230:231]
	v_addc_co_u32_e64 v233, s[34:35], 0, v233, s[96:97]
	s_waitcnt lgkmcnt(1)
	v_cmp_gt_u64_e64 s[88:89], v[226:227], v[230:231]
	v_addc_co_u32_e64 v233, s[34:35], 0, v233, s[84:85]
	s_waitcnt lgkmcnt(0)
	v_cmp_gt_u64_e64 s[90:91], v[228:229], v[230:231]
	v_addc_co_u32_e64 v233, s[34:35], 0, v233, s[86:87]
	v_addc_co_u32_e64 v233, s[34:35], 0, v233, s[88:89]
	v_addc_co_u32_e64 v233, s[34:35], 0, v233, s[90:91]
	v_mov_b32_e32 v80, v233
	v_readlane_b32 s30, v254, 51
	v_cmp_gt_u32_e32 vcc, 16, v80
	v_readlane_b32 s31, v254, 52
	s_and_b64 s[34:35], s[30:31], vcc
	v_cndmask_b32_e64 v80, 0, 1, s[34:35]
	v_readlane_b32 s30, v254, 47
	v_cmp_ne_u32_e32 vcc, 0, v80
	v_readlane_b32 s31, v254, 48
	s_and_saveexec_b64 s[34:35], s[30:31]
	s_cbranch_execz .LBB0_653
	v_lshl_add_u32 v79, v79, 2, 0
	v_readlane_b32 s30, v254, 53
	v_add_u32_e32 v80, 0x18800, v79
	v_mov_b32_e32 v79, vcc_hi
	v_mov_b32_e32 v81, vcc_lo
	v_readlane_b32 s31, v254, 54
	s_mov_b32 s58, 0
	s_mov_b64 vcc, exec
	v_cndmask_b32_e64 v79, v79, v81, s[30:31]
	ds_write_b32 v80, v79

.LBB0_864:
	s_or_b64 exec, exec, s[2:3]
	s_mov_b64 s[2:3], exec
	v_mbcnt_lo_u32_b32 v2, s2, 0
	v_mbcnt_hi_u32_b32 v2, s3, v2
	v_cmp_eq_u32_e32 vcc, 0, v2
	s_waitcnt vmcnt(0)
	s_and_saveexec_b64 s[4:5], vcc
	s_cbranch_execz .LBB0_866
	s_bcnt1_i32_b64 s2, s[2:3]
	v_mov_b32_e32 v2, s2
	v_readlane_b32 s2, v253, 55
	v_readlane_b32 s3, v253, 56
	s_nop 4
	global_atomic_add v3, v2, s[2:3]
.LBB0_866:
	s_or_b64 exec, exec, s[4:5]
	buffer_inv sc1
	s_waitcnt vmcnt(0)
	s_mov_b64 s[2:3], exec

.LBB0_1602:
	s_or_b64 exec, exec, s[4:5]
	s_mov_b64 s[4:5], exec
	v_mbcnt_lo_u32_b32 v2, s4, 0
	v_mbcnt_hi_u32_b32 v2, s5, v2
	v_cmp_eq_u32_e32 vcc, 0, v2
	s_waitcnt vmcnt(0)
	s_and_saveexec_b64 s[10:11], vcc
	s_cbranch_execz .LBB0_1604
	s_bcnt1_i32_b64 s4, s[4:5]
	v_mov_b32_e32 v2, s4
	v_readlane_b32 s4, v253, 55
	v_readlane_b32 s5, v253, 56
	s_nop 4
	global_atomic_add v3, v2, s[4:5]
.LBB0_1604:
	s_or_b64 exec, exec, s[10:11]
	buffer_inv sc1
	s_waitcnt vmcnt(0)
	s_mov_b64 s[4:5], exec
